# speedup vs baseline: 1.0130x; 1.0022x over previous
.Lh_stage1:
	s_setprio 2
	s_mov_b32 s47, 1
	s_mov_b32 s42, 0
	s_mov_b32 s43, 0
	s_mov_b32 m0, s46
	v_mov_b32_e32 v43, v39
	s_waitcnt vmcnt(1)
	v_cmp_lt_f32_e64 s[34:35], |v6|, s48
	v_cmp_lt_f32_e64 s[36:37], |v7|, s48
	v_cmp_lt_f32_e64 s[38:39], |v8|, s48
	v_cmp_lt_f32_e64 s[40:41], |v9|, s48
	s_and_b64 s[34:35], s[34:35], s[26:27]
	s_and_b64 s[36:37], s[36:37], s[28:29]
	s_and_b64 s[38:39], s[38:39], s[30:31]
	s_and_b64 s[40:41], s[40:41], s[32:33]
	v_mbcnt_lo_u32_b32 v28, s34, 0
	v_mbcnt_lo_u32_b32 v29, s36, 0
	v_mbcnt_lo_u32_b32 v30, s38, 0
	v_mbcnt_lo_u32_b32 v31, s40, 0
	v_mbcnt_hi_u32_b32 v28, s35, v28
	v_mbcnt_hi_u32_b32 v29, s37, v29
	v_mbcnt_hi_u32_b32 v30, s39, v30
	v_mbcnt_hi_u32_b32 v31, s41, v31
	s_bcnt1_i32_b64 s54, s[34:35]
	s_bcnt1_i32_b64 s55, s[36:37]
	s_bcnt1_i32_b64 s56, s[38:39]
	s_bcnt1_i32_b64 s57, s[40:41]
	s_lshl2_add_u32 s58, s42, s46
	v_lshl_add_u32 v28, v28, 2, s58
	s_lshl2_add_u32 s58, s54, s58
	v_lshl_add_u32 v29, v29, 2, s58
	s_lshl2_add_u32 s58, s55, s58
	v_lshl_add_u32 v30, v30, 2, s58
	s_lshl2_add_u32 s58, s56, s58
	v_lshl_add_u32 v31, v31, 2, s58
	s_add_i32 s54, s54, s55
	s_add_i32 s56, s56, s57
	s_add_i32 s42, s42, s54
	s_add_i32 s42, s42, s56
	s_mov_b64 exec, s[34:35]
	ds_write_b32 v28, v6
	s_mov_b64 exec, s[36:37]
	ds_write_b32 v29, v7
	s_mov_b64 exec, s[38:39]
	ds_write_b32 v30, v8
	s_mov_b64 exec, s[40:41]
	ds_write_b32 v31, v9
	s_mov_b64 exec, -1
	s_branch .Lh_loop_entry
.Lh_stage2:
	s_setprio 1
	s_mov_b32 s47, 2
	s_mov_b32 s42, 0
	s_mov_b32 s43, 0
	s_mov_b32 m0, s46
	v_mov_b32_e32 v43, v40
	s_waitcnt vmcnt(0)
	v_cmp_lt_f32_e64 s[34:35], |v10|, s48
	v_cmp_lt_f32_e64 s[36:37], |v11|, s48
	v_cmp_lt_f32_e64 s[38:39], |v12|, s48
	v_cmp_lt_f32_e64 s[40:41], |v13|, s48
	s_and_b64 s[34:35], s[34:35], s[26:27]
	s_and_b64 s[36:37], s[36:37], s[28:29]
	s_and_b64 s[38:39], s[38:39], s[30:31]
	s_and_b64 s[40:41], s[40:41], s[32:33]
	v_mbcnt_lo_u32_b32 v28, s34, 0
	v_mbcnt_lo_u32_b32 v29, s36, 0
	v_mbcnt_lo_u32_b32 v30, s38, 0
	v_mbcnt_lo_u32_b32 v31, s40, 0
	v_mbcnt_hi_u32_b32 v28, s35, v28
	v_mbcnt_hi_u32_b32 v29, s37, v29
	v_mbcnt_hi_u32_b32 v30, s39, v30
	v_mbcnt_hi_u32_b32 v31, s41, v31
	s_bcnt1_i32_b64 s54, s[34:35]
	s_bcnt1_i32_b64 s55, s[36:37]
	s_bcnt1_i32_b64 s56, s[38:39]
	s_bcnt1_i32_b64 s57, s[40:41]
	s_lshl2_add_u32 s58, s42, s46
	v_lshl_add_u32 v28, v28, 2, s58
	s_lshl2_add_u32 s58, s54, s58
	v_lshl_add_u32 v29, v29, 2, s58
	s_lshl2_add_u32 s58, s55, s58
	v_lshl_add_u32 v30, v30, 2, s58
	s_lshl2_add_u32 s58, s56, s58
	v_lshl_add_u32 v31, v31, 2, s58
	s_add_i32 s54, s54, s55
	s_add_i32 s56, s56, s57
	s_add_i32 s42, s42, s54
	s_add_i32 s42, s42, s56
	s_mov_b64 exec, s[34:35]
	ds_write_b32 v28, v10
	s_mov_b64 exec, s[36:37]
	ds_write_b32 v29, v11
	s_mov_b64 exec, s[38:39]
	ds_write_b32 v30, v12
	s_mov_b64 exec, s[40:41]
	ds_write_b32 v31, v13
	s_mov_b64 exec, -1
	s_branch .Lh_loop_entry

.Lh_loop_body:
	v_fmamk_f32 v27, v24, 0x42000000, v41
	ds_read_addtid_b32 v24 offset:256
	s_add_i32 s43, s43, 64
	v_rndne_f32_e32 v28, v27
	v_sub_f32_e32 v29, v27, v28
	v_cvt_i32_f32_e32 v30, v28
	v_mul_f32_e32 v37, 0xbf38aa3b, v29
	v_fmamk_f32 v32, v29, 0x3fb8aa3b, v42
	v_fma_f32 v33, -v29, s51, v42
	v_fmaak_f32 v31, v29, v37, 0x41a00000
	v_lshl_add_u32 v30, v30, 7, v43
	v_exp_f32_e32 v31, v31
	v_exp_f32_e32 v32, v32
	v_exp_f32_e32 v33, v33
	v_cvt_rpi_i32_f32_e32 v66, v31
	ds_add_u64 v30, v[66:67] offset:640
	v_mul_f32_e32 v34, v32, v31
	v_mul_f32_e32 v35, v33, v31
	v_cvt_rpi_i32_f32_e32 v57, v34
	v_cvt_rpi_i32_f32_e32 v64, v35
	v_mul_f32_e32 v32, 0x3ebc5ab2, v32
	v_mul_f32_e32 v33, 0x3ebc5ab2, v33
	v_mul_f32_e32 v34, v32, v34
	v_mul_f32_e32 v35, v33, v35
	v_cvt_rpi_i32_f32_e32 v59, v34
	v_cvt_rpi_i32_f32_e32 v62, v35
	v_mul_f32_e32 v32, 0x3ebc5ab2, v32
	v_mul_f32_e32 v33, 0x3ebc5ab2, v33
	v_mul_f32_e32 v34, v32, v34
	v_mul_f32_e32 v35, v33, v35
	v_cvt_rpi_i32_f32_e32 v61, v34
	v_cvt_rpi_i32_f32_e32 v60, v35
	ds_add_u64 v30, v[60:61] offset:256
	v_mul_f32_e32 v32, 0x3ebc5ab2, v32
	v_mul_f32_e32 v33, 0x3ebc5ab2, v33
	v_mul_f32_e32 v34, v32, v34
	v_mul_f32_e32 v35, v33, v35
	v_cvt_rpi_i32_f32_e32 v63, v34
	v_cvt_rpi_i32_f32_e32 v58, v35
	ds_add_u64 v30, v[62:63] offset:384
	ds_add_u64 v30, v[58:59] offset:128
	v_mul_f32_e32 v32, 0x3ebc5ab2, v32
	v_mul_f32_e32 v33, 0x3ebc5ab2, v33
	v_mul_f32_e32 v34, v32, v34
	v_mul_f32_e32 v35, v33, v35
	v_cvt_rpi_i32_f32_e32 v65, v34
	v_cvt_rpi_i32_f32_e32 v56, v35
	ds_add_u64 v30, v[64:65] offset:512
	ds_add_u64 v30, v[56:57]
	s_add_u32 m0, m0, 0x100
	s_sub_i32 s59, s42, s43
	s_cmp_ge_i32 s59, 64
	s_waitcnt lgkmcnt(6)
	s_cbranch_scc1 .Lh_loop_body
	s_cmp_lt_i32 s59, 1
	s_cbranch_scc1 .Lh_loop_exit
	s_bfm_b64 exec, s59, 0
	s_branch .Lh_loop_body
